# P2: S^T LDS fragment reads hoisted 5-8 deep with register-ring renaming (on top of chunk prefetch)
# speedup vs baseline: 1.0195x; 1.0124x over previous
.Lp2_nopf:
	s_andn2_b64 vcc, exec, s[26:27]
	ds_write_b16 v101, v186
	ds_write_b16_d16_hi v101, v186 offset:272
	ds_write_b16 v101, v187 offset:544
	ds_write_b16_d16_hi v101, v187 offset:816
	v_lshlrev_b32_e32 v3, 16, v186
	v_and_b32_e32 v54, 0xffff0000, v186
	v_lshlrev_b32_e32 v55, 16, v187
	v_mul_f32_e32 v3, v172, v3
	v_mul_f32_e32 v54, v172, v54
	v_mul_f32_e32 v55, v172, v55
	v_bfe_u32 v56, v3, 16, 1
	v_bfe_u32 v57, v54, 16, 1
	v_bfe_u32 v58, v55, 16, 1
	v_add3_u32 v3, v3, v56, s74
	v_add3_u32 v54, v54, v57, s74
	v_add3_u32 v55, v55, v58, s74
	ds_write_b16_d16_hi v102, v3
	ds_write_b16_d16_hi v102, v54 offset:272
	ds_write_b16_d16_hi v102, v55 offset:544
	v_and_b32_e32 v3, 0xffff0000, v187
	v_mul_f32_e32 v3, v172, v3
	v_bfe_u32 v54, v3, 16, 1
	v_add3_u32 v3, v3, v54, s74
	ds_write_b16_d16_hi v102, v3 offset:816
	ds_write_b16 v101, v4 offset:128
	ds_write_b16_d16_hi v101, v4 offset:400
	ds_write_b16 v101, v5 offset:672
	ds_write_b16_d16_hi v101, v5 offset:944
	v_lshlrev_b32_e32 v3, 16, v4
	v_mul_f32_e32 v3, v173, v3
	v_bfe_u32 v54, v3, 16, 1
	v_add3_u32 v3, v3, v54, s74
	ds_write_b16_d16_hi v102, v3 offset:128
	v_and_b32_e32 v3, 0xffff0000, v4
	v_mul_f32_e32 v3, v173, v3
	v_bfe_u32 v4, v3, 16, 1
	v_add3_u32 v3, v3, v4, s74
	ds_write_b16_d16_hi v102, v3 offset:400
	v_lshlrev_b32_e32 v3, 16, v5
	v_mul_f32_e32 v3, v173, v3
	v_bfe_u32 v4, v3, 16, 1
	v_add3_u32 v3, v3, v4, s74
	ds_write_b16_d16_hi v102, v3 offset:672
	v_and_b32_e32 v3, 0xffff0000, v5
	v_mul_f32_e32 v3, v173, v3
	v_bfe_u32 v4, v3, 16, 1
	v_add3_u32 v3, v3, v4, s74
	ds_write_b16_d16_hi v102, v3 offset:944
	v_cndmask_b32_e64 v3, 0, 1, s[26:27]
	v_cmp_ne_u32_e64 s[12:13], 1, v3
	v_mov_b32_e32 v57, 0
	v_mov_b32_e32 v56, 0
	v_mov_b32_e32 v55, 0
	v_mov_b32_e32 v54, 0
	s_waitcnt lgkmcnt(0)
	s_barrier
	s_cbranch_vccnz .LBB0_267
	ds_read_b128 v[62:65], v154
	ds_read_b128 v[66:69], v154 offset:4096
	ds_read_b128 v[70:73], v155
	ds_read_b128 v[174:177], v155 offset:4096
	ds_read_b128 v[178:181], v156
	ds_read_b128 v[182:185], v156 offset:4096
	ds_read_b128 v[186:189], v157
	ds_read_b128 v[190:193], v157 offset:4096
	s_andn2_b64 vcc, exec, s[2:3]
	s_nop 0
	s_waitcnt lgkmcnt(7)
	v_mfma_f32_16x16x32_bf16 v[54:57], v[62:65], v[50:53], 0
	ds_read_b128 v[62:65], v154 offset:32768
	s_nop 0
	s_waitcnt lgkmcnt(7)
	v_mfma_f32_16x16x32_bf16 v[58:61], v[66:69], v[50:53], 0
	ds_read_b128 v[66:69], v154 offset:36864
	s_nop 0
	s_waitcnt lgkmcnt(7)
	v_mfma_f32_16x16x32_bf16 v[54:57], v[70:73], v[46:49], v[54:57]
	ds_read_b128 v[70:73], v155 offset:32768
	s_nop 0
	s_waitcnt lgkmcnt(7)
	v_mfma_f32_16x16x32_bf16 v[58:61], v[174:177], v[46:49], v[58:61]
	ds_read_b128 v[174:177], v155 offset:36864
	s_nop 0
	s_waitcnt lgkmcnt(7)
	v_mfma_f32_16x16x32_bf16 v[54:57], v[178:181], v[42:45], v[54:57]
	ds_read_b128 v[178:181], v156 offset:32768
	s_nop 0
	s_waitcnt lgkmcnt(7)
	v_mfma_f32_16x16x32_bf16 v[58:61], v[182:185], v[42:45], v[58:61]
	ds_read_b128 v[182:185], v156 offset:36864
	s_nop 0
	s_waitcnt lgkmcnt(7)
	v_mfma_f32_16x16x32_bf16 v[54:57], v[186:189], v[38:41], v[54:57]
	ds_read_b128 v[186:189], v157 offset:32768
	s_nop 0
	s_waitcnt lgkmcnt(7)
	v_mfma_f32_16x16x32_bf16 v[58:61], v[190:193], v[38:41], v[58:61]
	ds_read_b128 v[190:193], v157 offset:36864
	s_nop 0
	s_waitcnt lgkmcnt(7)
	v_mfma_f32_16x16x32_bf16 v[54:57], v[62:65], v[34:37], v[54:57]
	s_nop 0
	s_waitcnt lgkmcnt(5)
	v_mfma_f32_16x16x32_bf16 v[54:57], v[70:73], v[30:33], v[54:57]
	s_nop 0
	s_waitcnt lgkmcnt(3)
	v_mfma_f32_16x16x32_bf16 v[54:57], v[178:181], v[26:29], v[54:57]
	v_mfma_f32_16x16x32_bf16 v[58:61], v[66:69], v[34:37], v[58:61]
	s_nop 0
	s_waitcnt lgkmcnt(1)
	v_mfma_f32_16x16x32_bf16 v[54:57], v[186:189], v[22:25], v[54:57]
	v_mfma_f32_16x16x32_bf16 v[58:61], v[174:177], v[30:33], v[58:61]
	s_nop 6
	v_mul_f32_e32 v3, v54, v160
	v_mul_f32_e32 v5, v56, v160
	v_mul_f32_e32 v54, v57, v160
	v_mfma_f32_16x16x32_bf16 v[56:59], v[182:185], v[26:29], v[58:61]
	v_mul_f32_e32 v4, v55, v160
	v_mul_f32_e32 v3, v3, v168
	v_mul_f32_e32 v4, v4, v169
	s_nop 0
	s_waitcnt lgkmcnt(0)
	v_mfma_f32_16x16x32_bf16 v[58:61], v[190:193], v[22:25], v[56:59]
	v_mul_f32_e32 v5, v5, v170
	v_mul_f32_e32 v55, v54, v171
	s_cbranch_vccnz .LBB0_263
	v_cndmask_b32_e64 v3, 0, v3, s[4:5]
	v_cndmask_b32_e64 v4, 0, v4, s[6:7]
	v_cndmask_b32_e64 v5, 0, v5, s[8:9]
	v_cndmask_b32_e64 v55, 0, v55, s[10:11]

.LBB0_267:
	v_cndmask_b32_e64 v3, 0, 1, s[30:31]
	v_mov_b32_e32 v61, 0
	v_cmp_ne_u32_e64 s[14:15], 1, v3
	s_andn2_b64 vcc, exec, s[30:31]
	v_mov_b32_e32 v60, 0
	v_mov_b32_e32 v59, 0
	v_mov_b32_e32 v58, 0
	s_cbranch_vccnz .LBB0_274
	ds_read_b128 v[66:69], v154 offset:8192
	ds_read_b128 v[70:73], v154 offset:12288
	ds_read_b128 v[174:177], v155 offset:8192
	ds_read_b128 v[178:181], v155 offset:12288
	ds_read_b128 v[182:185], v156 offset:8192
	ds_read_b128 v[186:189], v156 offset:12288
	ds_read_b128 v[190:193], v157 offset:8192
	s_andn2_b64 vcc, exec, s[34:35]
	s_nop 0
	s_waitcnt lgkmcnt(6)
	v_mfma_f32_16x16x32_bf16 v[58:61], v[66:69], v[50:53], 0
	ds_read_b128 v[66:69], v157 offset:12288
	s_nop 0
	s_waitcnt lgkmcnt(6)
	v_mfma_f32_16x16x32_bf16 v[62:65], v[70:73], v[50:53], 0
	ds_read_b128 v[70:73], v154 offset:40960
	s_nop 0
	s_waitcnt lgkmcnt(6)
	v_mfma_f32_16x16x32_bf16 v[58:61], v[174:177], v[46:49], v[58:61]
	ds_read_b128 v[174:177], v154 offset:45056
	s_nop 0
	s_waitcnt lgkmcnt(6)
	v_mfma_f32_16x16x32_bf16 v[62:65], v[178:181], v[46:49], v[62:65]
	ds_read_b128 v[178:181], v155 offset:40960
	s_nop 0
	s_waitcnt lgkmcnt(6)
	v_mfma_f32_16x16x32_bf16 v[58:61], v[182:185], v[42:45], v[58:61]
	ds_read_b128 v[182:185], v155 offset:45056
	s_nop 0
	s_waitcnt lgkmcnt(6)
	v_mfma_f32_16x16x32_bf16 v[62:65], v[186:189], v[42:45], v[62:65]
	ds_read_b128 v[186:189], v156 offset:40960
	s_nop 0
	s_waitcnt lgkmcnt(6)
	v_mfma_f32_16x16x32_bf16 v[58:61], v[190:193], v[38:41], v[58:61]
	ds_read_b128 v[190:193], v156 offset:45056
	s_nop 0
	s_waitcnt lgkmcnt(6)
	v_mfma_f32_16x16x32_bf16 v[62:65], v[66:69], v[38:41], v[62:65]
	ds_read_b128 v[66:69], v157 offset:40960
	s_nop 0
	s_waitcnt lgkmcnt(6)
	v_mfma_f32_16x16x32_bf16 v[58:61], v[70:73], v[34:37], v[58:61]
	ds_read_b128 v[70:73], v157 offset:45056
	s_nop 0
	s_waitcnt lgkmcnt(5)
	v_mfma_f32_16x16x32_bf16 v[58:61], v[178:181], v[30:33], v[58:61]
	s_nop 0
	s_waitcnt lgkmcnt(3)
	v_mfma_f32_16x16x32_bf16 v[58:61], v[186:189], v[26:29], v[58:61]
	v_mfma_f32_16x16x32_bf16 v[62:65], v[174:177], v[34:37], v[62:65]
	s_nop 0
	s_waitcnt lgkmcnt(1)
	v_mfma_f32_16x16x32_bf16 v[58:61], v[66:69], v[22:25], v[58:61]
	v_mfma_f32_16x16x32_bf16 v[62:65], v[182:185], v[30:33], v[62:65]
	s_nop 6
	v_mul_f32_e32 v3, v58, v162
	v_mul_f32_e32 v5, v60, v162
	v_mul_f32_e32 v58, v61, v162
	v_mfma_f32_16x16x32_bf16 v[60:63], v[190:193], v[26:29], v[62:65]
	v_mul_f32_e32 v4, v59, v162
	v_mul_f32_e32 v3, v3, v168
	v_mul_f32_e32 v4, v4, v169
	s_nop 0
	s_waitcnt lgkmcnt(0)
	v_mfma_f32_16x16x32_bf16 v[62:65], v[70:73], v[22:25], v[60:63]
	v_mul_f32_e32 v5, v5, v170
	v_mul_f32_e32 v59, v58, v171
	s_cbranch_vccnz .LBB0_270
	v_cndmask_b32_e64 v3, 0, v3, s[4:5]
	v_cndmask_b32_e64 v4, 0, v4, s[6:7]
	v_cndmask_b32_e64 v5, 0, v5, s[8:9]
	v_cndmask_b32_e64 v59, 0, v59, s[10:11]

.LBB0_274:
	v_cndmask_b32_e64 v3, 0, 1, s[40:41]
	v_mov_b32_e32 v65, 0
	v_cmp_ne_u32_e64 s[16:17], 1, v3
	s_andn2_b64 vcc, exec, s[40:41]
	v_mov_b32_e32 v64, 0
	v_mov_b32_e32 v63, 0
	v_mov_b32_e32 v62, 0
	s_cbranch_vccnz .LBB0_281
	ds_read_b128 v[70:73], v154 offset:16384
	ds_read_b128 v[174:177], v154 offset:20480
	ds_read_b128 v[178:181], v155 offset:16384
	ds_read_b128 v[182:185], v155 offset:20480
	ds_read_b128 v[186:189], v156 offset:16384
	ds_read_b128 v[190:193], v156 offset:20480
	s_andn2_b64 vcc, exec, s[42:43]
	s_nop 0
	s_waitcnt lgkmcnt(5)
	v_mfma_f32_16x16x32_bf16 v[62:65], v[70:73], v[50:53], 0
	ds_read_b128 v[70:73], v157 offset:16384
	s_nop 0
	s_waitcnt lgkmcnt(5)
	v_mfma_f32_16x16x32_bf16 v[66:69], v[174:177], v[50:53], 0
	ds_read_b128 v[174:177], v157 offset:20480
	s_nop 0
	s_waitcnt lgkmcnt(5)
	v_mfma_f32_16x16x32_bf16 v[62:65], v[178:181], v[46:49], v[62:65]
	ds_read_b128 v[178:181], v154 offset:49152
	s_nop 0
	s_waitcnt lgkmcnt(5)
	v_mfma_f32_16x16x32_bf16 v[66:69], v[182:185], v[46:49], v[66:69]
	ds_read_b128 v[182:185], v154 offset:53248
	s_nop 0
	s_waitcnt lgkmcnt(5)
	v_mfma_f32_16x16x32_bf16 v[62:65], v[186:189], v[42:45], v[62:65]
	ds_read_b128 v[186:189], v155 offset:49152
	s_nop 0
	s_waitcnt lgkmcnt(5)
	v_mfma_f32_16x16x32_bf16 v[66:69], v[190:193], v[42:45], v[66:69]
	ds_read_b128 v[190:193], v155 offset:53248
	s_nop 0
	s_waitcnt lgkmcnt(5)
	v_mfma_f32_16x16x32_bf16 v[62:65], v[70:73], v[38:41], v[62:65]
	ds_read_b128 v[70:73], v156 offset:49152
	s_nop 0
	s_waitcnt lgkmcnt(5)
	v_mfma_f32_16x16x32_bf16 v[66:69], v[174:177], v[38:41], v[66:69]
	ds_read_b128 v[174:177], v156 offset:53248
	s_nop 0
	s_waitcnt lgkmcnt(5)
	v_mfma_f32_16x16x32_bf16 v[62:65], v[178:181], v[34:37], v[62:65]
	ds_read_b128 v[178:181], v157 offset:49152
	s_nop 0
	s_waitcnt lgkmcnt(4)
	v_mfma_f32_16x16x32_bf16 v[62:65], v[186:189], v[30:33], v[62:65]
	ds_read_b128 v[186:189], v157 offset:53248
	s_nop 0
	s_waitcnt lgkmcnt(3)
	v_mfma_f32_16x16x32_bf16 v[62:65], v[70:73], v[26:29], v[62:65]
	v_mfma_f32_16x16x32_bf16 v[66:69], v[182:185], v[34:37], v[66:69]
	s_nop 0
	s_waitcnt lgkmcnt(1)
	v_mfma_f32_16x16x32_bf16 v[62:65], v[178:181], v[22:25], v[62:65]
	v_mfma_f32_16x16x32_bf16 v[66:69], v[190:193], v[30:33], v[66:69]
	s_nop 6
	v_mul_f32_e32 v3, v62, v164
	v_mul_f32_e32 v5, v64, v164
	v_mul_f32_e32 v62, v65, v164
	v_mfma_f32_16x16x32_bf16 v[64:67], v[174:177], v[26:29], v[66:69]
	v_mul_f32_e32 v4, v63, v164
	v_mul_f32_e32 v3, v3, v168
	v_mul_f32_e32 v4, v4, v169
	s_nop 0
	s_waitcnt lgkmcnt(0)
	v_mfma_f32_16x16x32_bf16 v[66:69], v[186:189], v[22:25], v[64:67]
	v_mul_f32_e32 v5, v5, v170
	v_mul_f32_e32 v63, v62, v171
	s_cbranch_vccnz .LBB0_277
	v_cndmask_b32_e64 v3, 0, v3, s[4:5]
	v_cndmask_b32_e64 v4, 0, v4, s[6:7]
	v_cndmask_b32_e64 v5, 0, v5, s[8:9]
	v_cndmask_b32_e64 v63, 0, v63, s[10:11]

.LBB0_281:
	v_cndmask_b32_e64 v3, 0, 1, s[48:49]
	v_mov_b32_e32 v69, 0
	v_cmp_ne_u32_e64 s[18:19], 1, v3
	s_andn2_b64 vcc, exec, s[48:49]
	v_mov_b32_e32 v68, 0
	v_mov_b32_e32 v67, 0
	v_mov_b32_e32 v66, 0
	s_cbranch_vccnz .LBB0_288
	ds_read_b128 v[174:177], v154 offset:24576
	ds_read_b128 v[178:181], v154 offset:28672
	ds_read_b128 v[182:185], v155 offset:24576
	ds_read_b128 v[186:189], v155 offset:28672
	ds_read_b128 v[190:193], v156 offset:24576
	s_andn2_b64 vcc, exec, s[50:51]
	s_nop 0
	s_waitcnt lgkmcnt(4)
	v_mfma_f32_16x16x32_bf16 v[66:69], v[174:177], v[50:53], 0
	ds_read_b128 v[174:177], v156 offset:28672
	s_nop 0
	s_waitcnt lgkmcnt(4)
	v_mfma_f32_16x16x32_bf16 v[70:73], v[178:181], v[50:53], 0
	ds_read_b128 v[178:181], v157 offset:24576
	s_nop 0
	s_waitcnt lgkmcnt(4)
	v_mfma_f32_16x16x32_bf16 v[66:69], v[182:185], v[46:49], v[66:69]
	ds_read_b128 v[182:185], v157 offset:28672
	s_nop 0
	s_waitcnt lgkmcnt(4)
	v_mfma_f32_16x16x32_bf16 v[70:73], v[186:189], v[46:49], v[70:73]
	ds_read_b128 v[186:189], v154 offset:57344
	s_nop 0
	s_waitcnt lgkmcnt(4)
	v_mfma_f32_16x16x32_bf16 v[66:69], v[190:193], v[42:45], v[66:69]
	ds_read_b128 v[190:193], v154 offset:61440
	s_nop 0
	s_waitcnt lgkmcnt(4)
	v_mfma_f32_16x16x32_bf16 v[70:73], v[174:177], v[42:45], v[70:73]
	ds_read_b128 v[174:177], v155 offset:57344
	s_nop 0
	s_waitcnt lgkmcnt(4)
	v_mfma_f32_16x16x32_bf16 v[66:69], v[178:181], v[38:41], v[66:69]
	ds_read_b128 v[178:181], v155 offset:61440
	s_nop 0
	s_waitcnt lgkmcnt(4)
	v_mfma_f32_16x16x32_bf16 v[70:73], v[182:185], v[38:41], v[70:73]
	ds_read_b128 v[182:185], v156 offset:57344
	s_nop 0
	s_waitcnt lgkmcnt(4)
	v_mfma_f32_16x16x32_bf16 v[66:69], v[186:189], v[34:37], v[66:69]
	ds_read_b128 v[186:189], v156 offset:61440
	s_nop 0
	s_waitcnt lgkmcnt(3)
	v_mfma_f32_16x16x32_bf16 v[66:69], v[174:177], v[30:33], v[66:69]
	ds_read_b128 v[174:177], v157 offset:57344
	s_nop 0
	s_waitcnt lgkmcnt(2)
	v_mfma_f32_16x16x32_bf16 v[66:69], v[182:185], v[26:29], v[66:69]
	ds_read_b128 v[182:185], v157 offset:61440
	v_mfma_f32_16x16x32_bf16 v[70:73], v[190:193], v[34:37], v[70:73]
	s_nop 0
	s_waitcnt lgkmcnt(1)
	v_mfma_f32_16x16x32_bf16 v[66:69], v[174:177], v[22:25], v[66:69]
	v_mfma_f32_16x16x32_bf16 v[70:73], v[178:181], v[30:33], v[70:73]
	s_nop 6
	v_mul_f32_e32 v3, v66, v166
	v_mul_f32_e32 v5, v68, v166
	v_mul_f32_e32 v66, v69, v166
	v_mfma_f32_16x16x32_bf16 v[68:71], v[186:189], v[26:29], v[70:73]
	v_mul_f32_e32 v4, v67, v166
	v_mul_f32_e32 v3, v3, v168
	v_mul_f32_e32 v4, v4, v169
	s_nop 0
	s_waitcnt lgkmcnt(0)
	v_mfma_f32_16x16x32_bf16 v[70:73], v[182:185], v[22:25], v[68:71]
	v_mul_f32_e32 v5, v5, v170
	v_mul_f32_e32 v67, v66, v171
	s_cbranch_vccnz .LBB0_284
	v_cndmask_b32_e64 v3, 0, v3, s[4:5]
	v_cndmask_b32_e64 v4, 0, v4, s[6:7]
	v_cndmask_b32_e64 v5, 0, v5, s[8:9]
	v_cndmask_b32_e64 v67, 0, v67, s[10:11]
